# layer-1 w_gu conversion catch-up split: upper half of grid before its layer-1 in-proj GEMM units, lower half after (phase re-dispatch through the router-phase catch-up site)
# baseline (speedup 1.0000x reference)
.LBB0_13:
	s_mov_b32 s89, s34
	s_cmp_lt_u32 s100, 5
	s_cbranch_scc1 .Lcu_top_norm
	s_cmp_gt_u32 s100, 6
	s_cbranch_scc1 .Lcu_top_norm
	s_mov_b32 s89, 13
.Lcu_top_norm:
	v_mov_b32_e32 v0, v1
	v_readlane_b32 s0, v253, 3
	v_mbcnt_lo_u32_b32 v0, -1, v0
	v_mbcnt_hi_u32_b32 v194, -1, v0
	s_cmp_lg_u32 s89, 0
	v_add_u32_e32 v192, s0, v194
	v_readlane_b32 s0, v253, 0
	s_mov_b32 s72, s0
	v_readlane_b32 s0, v253, 4
	v_readlane_b32 s1, v253, 5
	s_mov_b64 s[4:5], -1
	s_cbranch_scc1 .LBB0_14
	s_getpc_b64 s[98:99]

.LBB0_144:
	s_add_u32 s52, s46, 0x4e000000
	s_addc_u32 s5, s47, 0
	v_and_b32_e32 v0, 0xff, v192
	s_waitcnt vmcnt(0)
	v_mov_b32_e32 v2, 0
	s_andn2_b64 vcc, exec, s[36:37]
	s_cbranch_vccnz .LBB0_146
	s_lshl_b32 s4, s48, 2
	s_add_i32 s4, s4, 0
	s_add_i32 s4, s4, 0x20200
	v_mov_b32_e32 v2, s4
	ds_read2_b32 v[2:3], v2 offset1:80
	s_ashr_i32 s49, s48, 31
	s_lshl_b64 s[14:15], s[48:49], 16
	s_add_u32 s14, s52, s14
	s_addc_u32 s15, s5, s15
	s_waitcnt lgkmcnt(0)
	v_sub_u32_e32 v2, s78, v2
	v_lshl_or_b32 v4, v2, 8, v0
	v_ashrrev_i32_e32 v5, 31, v4
	s_waitcnt vmcnt(14)
	v_lshl_add_u64 v[6:7], v[4:5], 2, s[14:15]
	v_cmp_lt_i32_e32 vcc, v4, v3
	v_mov_b32_e32 v2, 0
	s_and_saveexec_b64 s[100:101], vcc
	global_load_dword v2, v[6:7], off
	s_or_b64 exec, exec, s[100:101]
	s_mov_b32 s100, 0

.LBB0_154:
	v_mov_b32_e32 v3, 0
	s_andn2_b64 vcc, exec, s[36:37]
	s_cbranch_vccnz .LBB0_156
	s_lshl_b32 s4, s48, 2
	s_add_i32 s4, s4, 0
	s_add_i32 s4, s4, 0x20200
	v_mov_b32_e32 v3, s4
	ds_read2_b32 v[4:5], v3 offset1:80
	s_ashr_i32 s49, s48, 31
	s_lshl_b64 s[14:15], s[48:49], 16
	s_add_u32 s14, s52, s14
	s_addc_u32 s15, s5, s15
	s_waitcnt lgkmcnt(0)
	v_sub_u32_e32 v3, s78, v4
	s_waitcnt vmcnt(14)
	v_lshl_or_b32 v6, v3, 8, v0
	v_ashrrev_i32_e32 v7, 31, v6
	v_lshl_add_u64 v[8:9], v[6:7], 2, s[14:15]
	v_cmp_lt_i32_e32 vcc, v6, v5
	v_mov_b32_e32 v3, 0
	s_and_saveexec_b64 s[100:101], vcc
	global_load_dword v3, v[8:9], off
	s_or_b64 exec, exec, s[100:101]
	s_mov_b32 s100, 0

.LBB0_164:
	v_mov_b32_e32 v4, 0
	s_andn2_b64 vcc, exec, s[36:37]
	s_cbranch_vccnz .LBB0_166
	s_lshl_b32 s4, s48, 2
	s_add_i32 s4, s4, 0
	s_add_i32 s4, s4, 0x20200
	v_mov_b32_e32 v4, s4
	ds_read2_b32 v[4:5], v4 offset1:80
	s_ashr_i32 s49, s48, 31
	s_lshl_b64 s[14:15], s[48:49], 16
	s_add_u32 s14, s52, s14
	s_addc_u32 s15, s5, s15
	s_waitcnt lgkmcnt(0)
	v_sub_u32_e32 v4, s78, v4
	s_waitcnt vmcnt(14)
	v_lshl_or_b32 v6, v4, 8, v0
	v_ashrrev_i32_e32 v7, 31, v6
	v_lshl_add_u64 v[8:9], v[6:7], 2, s[14:15]
	v_cmp_lt_i32_e32 vcc, v6, v5
	v_mov_b32_e32 v4, 0
	s_and_saveexec_b64 s[100:101], vcc
	global_load_dword v4, v[8:9], off
	s_or_b64 exec, exec, s[100:101]
	s_mov_b32 s100, 0

.LBB0_174:
	v_mov_b32_e32 v5, 0
	s_andn2_b64 vcc, exec, s[36:37]
	s_cbranch_vccnz .LBB0_176
	s_lshl_b32 s4, s48, 2
	s_add_i32 s4, s4, 0
	s_add_i32 s4, s4, 0x20200
	v_mov_b32_e32 v5, s4
	s_waitcnt vmcnt(14)
	ds_read2_b32 v[6:7], v5 offset1:80
	s_ashr_i32 s49, s48, 31
	s_lshl_b64 s[14:15], s[48:49], 16
	s_add_u32 s14, s52, s14
	s_addc_u32 s15, s5, s15
	s_waitcnt lgkmcnt(0)
	v_sub_u32_e32 v5, s78, v6
	v_lshl_or_b32 v8, v5, 8, v0
	v_ashrrev_i32_e32 v9, 31, v8
	s_waitcnt vmcnt(13)
	v_lshl_add_u64 v[10:11], v[8:9], 2, s[14:15]
	v_cmp_lt_i32_e32 vcc, v8, v7
	v_mov_b32_e32 v5, 0
	s_and_saveexec_b64 s[100:101], vcc
	global_load_dword v5, v[10:11], off
	s_or_b64 exec, exec, s[100:101]
	s_mov_b32 s100, 0

.LBB0_184:
	s_waitcnt vmcnt(14)
	v_mov_b32_e32 v6, 0
	s_andn2_b64 vcc, exec, s[36:37]
	s_cbranch_vccnz .LBB0_186
	s_lshl_b32 s4, s48, 2
	s_add_i32 s4, s4, 0
	s_add_i32 s4, s4, 0x20200
	v_mov_b32_e32 v6, s4
	ds_read2_b32 v[6:7], v6 offset1:80
	s_ashr_i32 s49, s48, 31
	s_lshl_b64 s[14:15], s[48:49], 16
	s_add_u32 s14, s52, s14
	s_addc_u32 s15, s5, s15
	s_waitcnt lgkmcnt(0)
	v_sub_u32_e32 v6, s78, v6
	v_lshl_or_b32 v8, v6, 8, v0
	v_ashrrev_i32_e32 v9, 31, v8
	s_waitcnt vmcnt(13)
	v_lshl_add_u64 v[10:11], v[8:9], 2, s[14:15]
	v_cmp_lt_i32_e32 vcc, v8, v7
	v_mov_b32_e32 v6, 0
	s_and_saveexec_b64 s[100:101], vcc
	global_load_dword v6, v[10:11], off
	s_or_b64 exec, exec, s[100:101]
	s_mov_b32 s100, 0

.LBB0_194:
	v_mov_b32_e32 v7, 0
	s_andn2_b64 vcc, exec, s[36:37]
	s_cbranch_vccnz .LBB0_196
	s_lshl_b32 s4, s48, 2
	s_add_i32 s4, s4, 0
	s_add_i32 s4, s4, 0x20200
	v_mov_b32_e32 v7, s4
	ds_read2_b32 v[8:9], v7 offset1:80
	s_ashr_i32 s49, s48, 31
	s_lshl_b64 s[14:15], s[48:49], 16
	s_add_u32 s14, s52, s14
	s_addc_u32 s15, s5, s15
	s_waitcnt lgkmcnt(0)
	v_sub_u32_e32 v7, s78, v8
	s_waitcnt vmcnt(13)
	v_lshl_or_b32 v10, v7, 8, v0
	v_ashrrev_i32_e32 v11, 31, v10
	v_lshl_add_u64 v[12:13], v[10:11], 2, s[14:15]
	v_cmp_lt_i32_e32 vcc, v10, v9
	v_mov_b32_e32 v7, 0
	s_and_saveexec_b64 s[100:101], vcc
	global_load_dword v7, v[12:13], off
	s_or_b64 exec, exec, s[100:101]
	s_mov_b32 s100, 0

.LBB0_204:
	v_mov_b32_e32 v8, 0
	s_andn2_b64 vcc, exec, s[36:37]
	s_cbranch_vccnz .LBB0_206
	s_lshl_b32 s4, s48, 2
	s_add_i32 s4, s4, 0
	s_add_i32 s4, s4, 0x20200
	v_mov_b32_e32 v8, s4
	ds_read2_b32 v[8:9], v8 offset1:80
	s_ashr_i32 s49, s48, 31
	s_lshl_b64 s[14:15], s[48:49], 16
	s_add_u32 s14, s52, s14
	s_addc_u32 s15, s5, s15
	s_waitcnt lgkmcnt(0)
	v_sub_u32_e32 v8, s78, v8
	s_waitcnt vmcnt(13)
	v_lshl_or_b32 v10, v8, 8, v0
	v_ashrrev_i32_e32 v11, 31, v10
	v_lshl_add_u64 v[12:13], v[10:11], 2, s[14:15]
	v_cmp_lt_i32_e32 vcc, v10, v9
	v_mov_b32_e32 v8, 0
	s_and_saveexec_b64 s[100:101], vcc
	global_load_dword v8, v[12:13], off
	s_or_b64 exec, exec, s[100:101]
	s_mov_b32 s100, 0

.LBB0_214:
	v_mov_b32_e32 v9, 0
	s_andn2_b64 vcc, exec, s[36:37]
	s_cbranch_vccnz .LBB0_216
	s_lshl_b32 s4, s48, 2
	s_add_i32 s4, s4, 0
	s_add_i32 s4, s4, 0x20200
	v_mov_b32_e32 v9, s4
	s_waitcnt vmcnt(13)
	ds_read2_b32 v[10:11], v9 offset1:80
	s_ashr_i32 s49, s48, 31
	s_lshl_b64 s[14:15], s[48:49], 16
	s_add_u32 s14, s52, s14
	s_addc_u32 s15, s5, s15
	s_waitcnt lgkmcnt(0)
	v_sub_u32_e32 v9, s78, v10
	v_lshl_or_b32 v12, v9, 8, v0
	v_ashrrev_i32_e32 v13, 31, v12
	s_waitcnt vmcnt(12)
	v_lshl_add_u64 v[14:15], v[12:13], 2, s[14:15]
	v_cmp_lt_i32_e32 vcc, v12, v11
	v_mov_b32_e32 v9, 0
	s_and_saveexec_b64 s[100:101], vcc
	global_load_dword v9, v[14:15], off
	s_or_b64 exec, exec, s[100:101]
	s_mov_b32 s100, 0

.LBB0_224:
	s_waitcnt vmcnt(13)
	v_mov_b32_e32 v10, 0
	s_andn2_b64 vcc, exec, s[36:37]
	s_cbranch_vccnz .LBB0_226
	s_lshl_b32 s4, s48, 2
	s_add_i32 s4, s4, 0
	s_add_i32 s4, s4, 0x20200
	v_mov_b32_e32 v10, s4
	ds_read2_b32 v[10:11], v10 offset1:80
	s_ashr_i32 s49, s48, 31
	s_lshl_b64 s[14:15], s[48:49], 16
	s_add_u32 s4, s52, s14
	s_addc_u32 s5, s5, s15
	s_waitcnt lgkmcnt(0)
	v_sub_u32_e32 v10, s78, v10
	v_lshl_or_b32 v12, v10, 8, v0
	v_ashrrev_i32_e32 v13, 31, v12
	s_waitcnt vmcnt(12)
	v_lshl_add_u64 v[14:15], v[12:13], 2, s[4:5]
	v_cmp_lt_i32_e32 vcc, v12, v11
	v_mov_b32_e32 v10, 0
	s_and_saveexec_b64 s[100:101], vcc
	global_load_dword v10, v[14:15], off
	s_or_b64 exec, exec, s[100:101]
	s_mov_b32 s100, 0

.LBB0_405:
	s_cmp_gt_i32 s91, 3
	s_mov_b64 s[26:27], -1
	s_cbranch_scc0 .LBB0_492
	s_add_i32 s4, s89, -9
	v_readlane_b32 s62, v254, 7
	v_readlane_b32 s64, v254, 11
	v_readlane_b32 s68, v254, 63
	s_cmp_gt_u32 s4, 7
	v_readlane_b32 s61, v253, 19
	v_readlane_b32 s63, v254, 8
	v_readlane_b32 s65, v254, 12
	s_movk_i32 s66, 0xbff
	v_readlane_b32 s69, v255, 0
	s_cbranch_scc1 .LBB0_476
	s_cmp_eq_u32 s100, 5
	s_cselect_b32 s66, s101, s66
	s_load_dwordx2 s[26:27], s[0:1], 0x98
	v_cmp_eq_u32_e64 s[38:39], 0, v192
	s_waitcnt lgkmcnt(0)
	s_barrier
	s_add_u32 s44, s26, 0x2000
	s_addc_u32 s45, s27, 0
	s_and_saveexec_b64 s[36:37], s[38:39]
	s_cbranch_execz .LBB0_413
	global_load_dword v2, v1, s[44:45] sc1
	v_mov_b32_e32 v0, 0x1000
	s_waitcnt vmcnt(0)
	v_cmp_lt_u32_e32 vcc, s66, v2
	s_cbranch_vccnz .LBB0_412
	s_mov_b64 s[42:43], exec
	v_mbcnt_lo_u32_b32 v0, s42, 0
	v_mbcnt_hi_u32_b32 v0, s43, v0
	v_cmp_eq_u32_e32 vcc, 0, v0
	s_and_saveexec_b64 s[40:41], vcc
	s_cbranch_execz .LBB0_411
	s_bcnt1_i32_b64 s4, s[42:43]
	v_mov_b32_e32 v2, s4
	global_atomic_add v2, v1, v2, s[44:45] sc0

.LBB0_476:
	s_cmp_lt_u32 s100, 5
	s_cbranch_scc1 .Lcu_476_norm
	s_cmp_eq_u32 s100, 5
	s_cselect_b32 s100, 3, 7
	s_waitcnt vmcnt(0) lgkmcnt(0)
	s_branch .LBB0_13

.LBB0_655:
	s_and_b64 vcc, exec, s[56:57]
	s_cbranch_vccz .LBB0_786
	v_ashrrev_i32_e32 v0, 31, v192
	v_lshrrev_b32_e32 v0, 26, v0
	v_add_u32_e32 v0, v192, v0
	v_ashrrev_i32_e32 v163, 6, v0
	v_bfe_i32 v0, v192, 27, 1
	v_lshlrev_b32_e32 v177, 4, v192
	v_lshrrev_b32_e32 v0, 22, v0
	v_add_u32_e32 v0, v177, v0
	v_and_b32_e32 v0, 0xfffffc00, v0
	v_sub_u32_e32 v0, v177, v0
	s_waitcnt vmcnt(0)
	v_lshrrev_b32_e32 v2, 4, v0
	v_bitop3_b32 v0, v2, v0, 32 bitop3:0x6c
	v_ashrrev_i32_e32 v3, 31, v0
	v_lshrrev_b32_e32 v3, 26, v3
	v_add_u32_e32 v3, v0, v3
	v_lshlrev_b32_e32 v2, 3, v163
	v_ashrrev_i32_e32 v181, 6, v3
	v_and_b32_e32 v3, 0xc0, v3
	v_and_b32_e32 v2, -16, v2
	v_sub_u32_e32 v0, v0, v3
	v_add_u32_e32 v2, v181, v2
	v_ashrrev_i16_sdwa v0, v225, sext(v0) dst_sel:DWORD dst_unused:UNUSED_PAD src0_sel:DWORD src1_sel:BYTE_0
	v_lshlrev_b32_e32 v4, 5, v163
	v_bfe_i32 v183, v0, 0, 16
	v_lshlrev_b32_e32 v0, 1, v2
	v_lshrrev_b32_e32 v3, 2, v2
	v_and_b32_e32 v5, 3, v181
	s_mov_b32 s4, 0x1fffe0
	v_and_b32_e32 v4, 32, v4
	v_and_b32_e32 v0, 24, v0
	v_and_b32_e32 v3, 4, v3
	v_and_or_b32 v5, v2, s4, v5
	v_or3_b32 v0, v5, v3, v0
	v_add_lshl_u32 v3, v4, v183, 1
	v_lshl_add_u32 v166, v0, 11, v3
	v_add_u32_e32 v0, 0x2000, v177
	v_lshl_add_u32 v164, v2, 11, v3
	v_ashrrev_i32_e32 v2, 31, v0
	v_lshrrev_b32_e32 v2, 22, v2
	v_add_u32_e32 v2, v0, v2
	v_ashrrev_i32_e32 v189, 10, v2
	v_mul_i32_i24_e32 v2, 0x400, v189
	v_sub_u32_e32 v0, v0, v2
	v_lshrrev_b32_e32 v2, 4, v0
	v_bitop3_b32 v0, v2, v0, 32 bitop3:0x6c
	v_ashrrev_i32_e32 v3, 31, v0
	v_lshrrev_b32_e32 v3, 26, v3
	v_add_u32_e32 v3, v0, v3
	v_lshlrev_b32_e32 v2, 3, v189
	v_ashrrev_i32_e32 v193, 6, v3
	v_and_b32_e32 v3, 0xc0, v3
	v_and_b32_e32 v2, -16, v2
	v_sub_u32_e32 v0, v0, v3
	s_load_dwordx2 s[30:31], s[0:1], 0x98
	v_add_u32_e32 v2, v193, v2
	v_ashrrev_i16_sdwa v0, v225, sext(v0) dst_sel:DWORD dst_unused:UNUSED_PAD src0_sel:DWORD src1_sel:BYTE_0
	v_lshlrev_b32_e32 v4, 5, v189
	v_bfe_i32 v195, v0, 0, 16
	v_lshlrev_b32_e32 v0, 1, v2
	v_lshrrev_b32_e32 v3, 2, v2
	v_and_b32_e32 v5, 3, v193
	s_add_i32 s89, s89, 6
	v_and_b32_e32 v4, 32, v4
	v_and_b32_e32 v0, 24, v0
	v_and_b32_e32 v3, 4, v3
	v_and_or_b32 v5, v2, s4, v5
	s_cmp_lt_u32 s89, 15
	v_or3_b32 v0, v5, v3, v0
	v_add_lshl_u32 v3, v4, v195, 1
	v_and_b32_e32 v179, 15, v194
	v_lshlrev_b32_e32 v162, 2, v194
	s_cselect_b64 s[40:41], -1, 0
	v_readfirstlane_b32 s6, v192
	v_lshl_add_u32 v168, v2, 11, v3
	v_lshl_add_u32 v170, v0, 11, v3
	v_lshlrev_b32_e32 v197, 6, v179
	s_cmp_lg_u32 s34, 9
	s_cbranch_scc1 .Lcu_a_not9
	s_cmp_eq_u32 s100, 7
	s_cbranch_scc1 .Lcu_a_fin
	s_cmp_lg_u32 s100, 0
	s_cbranch_scc1 .Les_a_norm
	v_readlane_b32 s101, v254, 30
	s_cmp_ge_i32 s72, s101
	s_cbranch_scc0 .Les_a_norm
	v_readlane_b32 s4, v255, 62
	v_readlane_b32 s5, v255, 61
	s_add_u32 s4, s4, 0x2000
	s_addc_u32 s5, s5, 0
	global_load_dword v0, v1, s[4:5] sc1
	s_waitcnt vmcnt(0)
	v_readfirstlane_b32 s4, v0
	s_add_i32 s4, s4, 0xc00
	s_lshr_b32 s4, s4, 1
	s_add_i32 s101, s4, -1
	s_mov_b32 s100, 5
	s_branch .Les_tramp
.Lcu_a_fin:
	s_mov_b32 s100, 4
	v_and_b32_e32 v205, 32, v162
	s_branch .LBB0_688
.Lcu_a_not9:
	s_cmp_lg_u32 s34, 1
	s_cbranch_scc1 .Les_a_norm
	s_cmp_lg_u32 s100, 0
	s_cbranch_scc1 .Les_a_norm
	v_readlane_b32 s101, v254, 30
	s_cmp_ge_i32 s72, s101
	s_cbranch_scc0 .Les_a_norm
	s_mov_b32 s100, 1
	v_and_b32_e32 v205, 32, v162
	s_branch .LBB0_688

.Lcu_post:
	s_cmp_lg_u32 s34, 9
	s_cbranch_scc1 .LBB0_786
	s_cmp_lg_u32 s100, 0
	s_cbranch_scc1 .Lcu_post_clr
	s_mov_b32 s100, 6
	s_waitcnt vmcnt(0) lgkmcnt(0)
	s_branch .Les_tramp
.Lcu_post_clr:
	s_mov_b32 s100, 0
	s_branch .LBB0_786
